# mixer-B softmax section: K/V LDS writes first (data landed a full section earlier), next staging loads issued right behind them instead of in the MFMA section
# speedup vs baseline: 1.0031x; 1.0031x over previous
; #define ATT_SBAR() __builtin_amdgcn_sched_barrier(0)
; #define ATT_PK4(P, BASE, OUT) do { u32x4 w = {cvtpk(P[BASE + 0], P[BASE + 1]), cvtpk(P[BASE + 2], P[BASE + 3]), cvtpk(P[BASE + 4], P[BASE + 5]), cvtpk(P[BASE + 6], P[BASE + 7])}; \
;     OUT = *reinterpret_cast<bf16x8*>(&w); } while (0)
; #define ATT_LOAD_K(t) do { const unsigned so_ = (unsigned)(t) * (unsigned)(KVBLK * LDK * 2); sk0 = __builtin_bit_cast(bf16x8, __builtin_amdgcn_raw_buffer_load_b128(krs, koff, so_, 0)); \
;     if constexpr (DQK == 128) sk1 = __builtin_bit_cast(bf16x8, __builtin_amdgcn_raw_buffer_load_b128(krs, koff, so_ + (unsigned)(32 * LDK * 2), 0)); } while (0)
; #define ATT_LOAD_V(t) do { const unsigned so_ = (unsigned)(t) * (unsigned)(KVBLK * LDV * 2); sv0 = __builtin_bit_cast(bf16x8, __builtin_amdgcn_raw_buffer_load_b128(vrs, voff, so_, 0)); \
;     sv1 = __builtin_bit_cast(bf16x8, __builtin_amdgcn_raw_buffer_load_b128(vrs, voff, so_ + (unsigned)(32 * LDV * 2), 0)); } while (0)
; #define ATT_WRITE_K(so) do { *(bf16x8*)(K_lds + (so) + kswz<DQK>(kr, kc * 2)) = sk0; if constexpr (DQK == 128) *(bf16x8*)(K_lds + (so) + kswz<DQK>(32 + kr, kc * 2)) = sk1; } while (0)
; #define ATT_WRITE_V(so) do { *(bf16x8*)(V_lds + (so) + vst0) = sv0; *(bf16x8*)(V_lds + (so) + vst1) = sv1; } while (0)
; #define ATT_BAR() do { ATT_SBAR(); asm volatile("s_barrier" ::: "memory"); ATT_SBAR(); } while (0)
; #define ATT_VPAIR(buf, so, blk, ks) do { if constexpr (!(ABL & 8) && !(ABL & 32)) { buf[2 * (ks)] = vtr(vq0 + (so) + v_rd_off(blk, ks, 0)); buf[2 * (ks) + 1] = vtr(vq0 + (so) + v_rd_off(blk, ks, 1)); } } while (0)
; __device__ __forceinline__ void softmax_exp_pack(f32x16& p0, f32x16& p1, bf16x8& pa0, bf16x8& pa1, bf16x8& pa2, bf16x8& pa3) {
;     ...
;   for (int r = 0; r < 16; ++r) { p0[r] = __builtin_amdgcn_exp2f(p0[r]); p1[r] = __builtin_amdgcn_exp2f(p1[r]); }
;     ...
;   ATT_PK4(p0, 0, pa0); ATT_PK4(p0, 8, pa1); ATT_PK4(p1, 0, pa2); ATT_PK4(p1, 8, pa3);
;     ...
;     if constexpr (!(ABL & 4)) { ATT_WRITE_K(k2); ATT_WRITE_V(v1); }
;     ATT_SBAR();
; #pragma unroll
;     for (int ks = 0; ks < 4; ++ks) ATT_VPAIR(va, v0, 0, ks);
;     asm volatile("s_waitcnt lgkmcnt(8)" ::: "memory"); ATT_BAR();
;     ATT_XSECTION(true);
;     if constexpr (!(ABL & 4)) { const int tk = (t + 3 < NT) ? t + 3 : NT - 1, tv = (t + 2 < NT) ? t + 2 : NT - 1; ATT_LOAD_K(tk); ATT_LOAD_V(tv); }
.LBB0_283:
	v_add_u32_e32 v152, s94, v169
	v_add_u32_e32 v153, s95, v167
	v_add_u32_e32 v154, s95, v168
	s_waitcnt vmcnt(0)
	ds_write_b128 v152, v[224:227] offset:49152
	ds_write_b128 v153, v[228:231]
	ds_write_b128 v154, v[232:235]
	s_min_u32 s14, s97, 0x7c
	s_lshl_b32 s14, s14, 17
	s_add_i32 s14, s14, 0x60000
	buffer_load_dwordx4 v[224:227], v170, s[8:11], s14 offen
	s_add_i32 s19, s36, 0xffff0000
	s_mov_b32 s14, s10
	s_mov_b32 s15, s11
	buffer_load_dwordx4 v[228:231], v171, s[12:15], s19 offen
	buffer_load_dwordx4 v[232:235], v171, s[12:15], s36 offen
	v_exp_f32_e32 v98, v98
	v_exp_f32_e32 v114, v114
	v_exp_f32_e32 v99, v99
	v_exp_f32_e32 v115, v115
	v_exp_f32_e32 v100, v100
	v_exp_f32_e32 v101, v101
	v_exp_f32_e32 v102, v102
	v_exp_f32_e32 v103, v103
	v_exp_f32_e32 v106, v106
	v_exp_f32_e32 v107, v107
	v_exp_f32_e32 v116, v116
	v_exp_f32_e32 v117, v117
	v_exp_f32_e32 v118, v118
	v_exp_f32_e32 v119, v119
	v_exp_f32_e32 v104, v104
	v_exp_f32_e32 v120, v120
	v_exp_f32_e32 v105, v105
	v_exp_f32_e32 v121, v121
	v_exp_f32_e32 v122, v122
	v_exp_f32_e32 v123, v123
	v_exp_f32_e32 v108, v108
	v_exp_f32_e32 v124, v124
	v_exp_f32_e32 v109, v109
	v_exp_f32_e32 v125, v125
	v_exp_f32_e32 v110, v110
	v_exp_f32_e32 v126, v126
	v_exp_f32_e32 v111, v111
	v_exp_f32_e32 v127, v127
	v_exp_f32_e32 v112, v112
	v_exp_f32_e32 v128, v128
	v_exp_f32_e32 v113, v113
	v_exp_f32_e32 v129, v129
	v_cvt_pk_bf16_f32 v2, v98, v99
	v_cvt_pk_bf16_f32 v3, v100, v101
	v_cvt_pk_bf16_f32 v4, v102, v103
	v_cvt_pk_bf16_f32 v6, v106, v107
	v_cvt_pk_bf16_f32 v10, v114, v115
	v_cvt_pk_bf16_f32 v5, v104, v105
	v_cvt_pk_bf16_f32 v7, v108, v109
	v_cvt_pk_bf16_f32 v8, v110, v111
	v_cvt_pk_bf16_f32 v9, v112, v113
	v_cvt_pk_bf16_f32 v11, v116, v117
	v_cvt_pk_bf16_f32 v12, v118, v119
	v_cvt_pk_bf16_f32 v13, v120, v121
	v_cvt_pk_bf16_f32 v14, v122, v123
	v_cvt_pk_bf16_f32 v15, v124, v125
	v_cvt_pk_bf16_f32 v16, v126, v127
	v_cvt_pk_bf16_f32 v17, v128, v129
	v_add_u32_e32 v249, s96, v172
	ds_read_b128 v[152:155], v249 offset:49152
	ds_read_b128 v[156:159], v249 offset:53760
	ds_read_b128 v[160:163], v249 offset:49184
	ds_read_b128 v[176:179], v249 offset:53792
	s_waitcnt lgkmcnt(4)
	s_barrier
; #define ATT_SBAR() __builtin_amdgcn_sched_barrier(0)
; __device__ __forceinline__ unsigned cvtpk(float lo, float hi) { f32x2_t v = {lo, hi}; bf16x2_t b = __builtin_convertvector(v, bf16x2_t); return __builtin_bit_cast(unsigned, b); }
; #define ATT_LOAD_K(t) do { const unsigned so_ = (unsigned)(t) * (unsigned)(KVBLK * LDK * 2); sk0 = __builtin_bit_cast(bf16x8, __builtin_amdgcn_raw_buffer_load_b128(krs, koff, so_, 0)); \
;     if constexpr (DQK == 128) sk1 = __builtin_bit_cast(bf16x8, __builtin_amdgcn_raw_buffer_load_b128(krs, koff, so_ + (unsigned)(32 * LDK * 2), 0)); } while (0)
; #define ATT_LOAD_V(t) do { const unsigned so_ = (unsigned)(t) * (unsigned)(KVBLK * LDV * 2); sv0 = __builtin_bit_cast(bf16x8, __builtin_amdgcn_raw_buffer_load_b128(vrs, voff, so_, 0)); \
;     sv1 = __builtin_bit_cast(bf16x8, __builtin_amdgcn_raw_buffer_load_b128(vrs, voff, so_ + (unsigned)(32 * LDV * 2), 0)); } while (0)
; #define ATT_WRITE_K(so) do { *(bf16x8*)(K_lds + (so) + kswz<DQK>(kr, kc * 2)) = sk0; if constexpr (DQK == 128) *(bf16x8*)(K_lds + (so) + kswz<DQK>(32 + kr, kc * 2)) = sk1; } while (0)
;     ...
;   for (int t = 0; t + 1 < NT; ++t) {
;     if constexpr (ABL & 1) { u32x4 w0 = {cvtpk(p0[0], p0[1]), cvtpk(p0[2], p0[3]), cvtpk(p0[4], p0[5]), cvtpk(p0[6], p0[7])}, w1 = {cvtpk(p0[8], p0[9]), cvtpk(p0[10], p0[11]), cvtpk(p0[12], p0[13]), cvtpk(p0[14], p0[15])};
;         u32x4 w2 = {cvtpk(p1[0], p1[1]), cvtpk(p1[2], p1[3]), cvtpk(p1[4], p1[5]), cvtpk(p1[6], p1[7])}, w3 = {cvtpk(p1[8], p1[9]), cvtpk(p1[10], p1[11]), cvtpk(p1[12], p1[13]), cvtpk(p1[14], p1[15])};
;         pa0 = *reinterpret_cast<bf16x8*>(&w0); pa1 = *reinterpret_cast<bf16x8*>(&w1); pa2 = *reinterpret_cast<bf16x8*>(&w2); pa3 = *reinterpret_cast<bf16x8*>(&w3); }
;     else { ATT_SOFTMAX(t == 0); }
;     if constexpr (!(ABL & 4)) { ATT_WRITE_K(k2); ATT_WRITE_V(v1); }
;     ATT_SBAR();
; #pragma unroll
;     for (int ks = 0; ks < 4; ++ks) ATT_VPAIR(va, v0, 0, ks);
;     asm volatile("s_waitcnt lgkmcnt(8)" ::: "memory"); ATT_BAR();
;     ATT_XSECTION(true);
;     if constexpr (!(ABL & 4)) { const int tk = (t + 3 < NT) ? t + 3 : NT - 1, tv = (t + 2 < NT) ? t + 2 : NT - 1; ATT_LOAD_K(tk); ATT_LOAD_V(tv); }
;     ATT_BAR();
;     { const int tk_ = k0; k0 = k1; k1 = k2; k2 = tk_; const int tv_ = v0; v0 = v1; v1 = v2; v2 = tv_; }
	s_setprio 2
	s_waitcnt lgkmcnt(3)
	v_mfma_f32_32x32x16_bf16 v[98:113], v[152:155], v[136:139], v[82:97]
	ds_read_b128 v[180:183], v249 offset:49216
	s_waitcnt lgkmcnt(3)
	v_mfma_f32_32x32x16_bf16 v[114:129], v[156:159], v[136:139], v[82:97]
	ds_read_b128 v[186:189], v249 offset:53824
	v_add_u32_e32 v248, s37, v131
	s_waitcnt lgkmcnt(3)
	v_mfma_f32_32x32x16_bf16 v[98:113], v[160:163], v[140:143], v[98:113]
	ds_read_b128 v[190:193], v249 offset:49248
	ds_read_b64_tr_b16 v[198:199], v248
	ds_read_b64_tr_b16 v[200:201], v248 offset:2048
	s_waitcnt lgkmcnt(5)
	v_mfma_f32_32x32x16_bf16 v[114:129], v[176:179], v[140:143], v[114:129]
	ds_read_b128 v[194:197], v249 offset:53856
	ds_read_b64_tr_b16 v[212:213], v248 offset:4096
	ds_read_b64_tr_b16 v[214:215], v248 offset:6144
	s_waitcnt lgkmcnt(7)
	v_mfma_f32_32x32x16_bf16 v[98:113], v[180:183], v[144:147], v[98:113]
	ds_read_b64_tr_b16 v[216:217], v248 offset:8192
	ds_read_b64_tr_b16 v[218:219], v248 offset:10240
	s_waitcnt lgkmcnt(8)
	v_mfma_f32_32x32x16_bf16 v[114:129], v[186:189], v[144:147], v[114:129]
	ds_read_b64_tr_b16 v[220:221], v248 offset:12288
	ds_read_b64_tr_b16 v[222:223], v248 offset:14336
	s_waitcnt lgkmcnt(9)
	v_mfma_f32_32x32x16_bf16 v[98:113], v[190:193], v[148:151], v[98:113]
	s_waitcnt lgkmcnt(6)
	v_mfma_f32_32x32x16_bf16 v[114:129], v[194:197], v[148:151], v[114:129]
	v_mfma_f32_32x32x16_bf16 v[18:33], v[2:5], v[198:201], v[18:33]
	ds_read_b64_tr_b16 v[236:237], v248 offset:512
	ds_read_b64_tr_b16 v[238:239], v248 offset:2560
	s_waitcnt lgkmcnt(6)
	v_mfma_f32_32x32x16_bf16 v[18:33], v[6:9], v[212:215], v[18:33]
	ds_read_b64_tr_b16 v[198:199], v248 offset:4608
	ds_read_b64_tr_b16 v[200:201], v248 offset:6656
	s_waitcnt lgkmcnt(6)
	v_mfma_f32_32x32x16_bf16 v[18:33], v[10:13], v[216:219], v[18:33]
	ds_read_b64_tr_b16 v[212:213], v248 offset:8704
	ds_read_b64_tr_b16 v[214:215], v248 offset:10752
	s_waitcnt lgkmcnt(6)
	v_mfma_f32_32x32x16_bf16 v[18:33], v[14:17], v[220:223], v[18:33]
	ds_read_b64_tr_b16 v[216:217], v248 offset:12800
	ds_read_b64_tr_b16 v[218:219], v248 offset:14848
	v_max3_f32 v249, v98, v99, v100
	s_waitcnt lgkmcnt(6)
	v_mfma_f32_32x32x16_bf16 v[34:49], v[2:5], v[236:239], v[34:49]
	ds_read_b64_tr_b16 v[220:221], v248 offset:1024
	ds_read_b64_tr_b16 v[222:223], v248 offset:3072
	v_max3_f32 v173, v114, v115, v116
	s_waitcnt lgkmcnt(6)
	v_mfma_f32_32x32x16_bf16 v[34:49], v[6:9], v[198:201], v[34:49]
	ds_read_b64_tr_b16 v[236:237], v248 offset:5120
	ds_read_b64_tr_b16 v[238:239], v248 offset:7168
	v_max3_f32 v249, v249, v101, v102
	s_waitcnt lgkmcnt(6)
	v_mfma_f32_32x32x16_bf16 v[34:49], v[10:13], v[212:215], v[34:49]
	ds_read_b64_tr_b16 v[198:199], v248 offset:9216
	ds_read_b64_tr_b16 v[200:201], v248 offset:11264
	v_max3_f32 v173, v173, v117, v118
	s_waitcnt lgkmcnt(6)
	v_mfma_f32_32x32x16_bf16 v[34:49], v[14:17], v[216:219], v[34:49]
	ds_read_b64_tr_b16 v[212:213], v248 offset:13312
	ds_read_b64_tr_b16 v[214:215], v248 offset:15360
	v_max3_f32 v249, v249, v103, v104
	s_waitcnt lgkmcnt(6)
	v_mfma_f32_32x32x16_bf16 v[50:65], v[2:5], v[220:223], v[50:65]
	ds_read_b64_tr_b16 v[216:217], v248 offset:1536
	ds_read_b64_tr_b16 v[218:219], v248 offset:3584
	v_max3_f32 v173, v173, v119, v120
	s_waitcnt lgkmcnt(6)
	v_mfma_f32_32x32x16_bf16 v[50:65], v[6:9], v[236:239], v[50:65]
	ds_read_b64_tr_b16 v[220:221], v248 offset:5632
	ds_read_b64_tr_b16 v[222:223], v248 offset:7680
	v_max3_f32 v249, v249, v105, v106
	s_waitcnt lgkmcnt(6)
	v_mfma_f32_32x32x16_bf16 v[50:65], v[10:13], v[198:201], v[50:65]
	ds_read_b64_tr_b16 v[236:237], v248 offset:9728
	ds_read_b64_tr_b16 v[238:239], v248 offset:11776
	v_max3_f32 v173, v173, v121, v122
	s_waitcnt lgkmcnt(6)
	v_mfma_f32_32x32x16_bf16 v[50:65], v[14:17], v[212:215], v[50:65]
	ds_read_b64_tr_b16 v[198:199], v248 offset:13824
	ds_read_b64_tr_b16 v[200:201], v248 offset:15872
	v_max3_f32 v249, v249, v107, v108
	s_waitcnt lgkmcnt(6)
	v_mfma_f32_32x32x16_bf16 v[66:81], v[2:5], v[216:219], v[66:81]
	v_max3_f32 v173, v173, v123, v124
	s_waitcnt lgkmcnt(4)
	v_mfma_f32_32x32x16_bf16 v[66:81], v[6:9], v[220:223], v[66:81]
	v_max3_f32 v249, v249, v109, v110
	s_waitcnt lgkmcnt(2)
	v_mfma_f32_32x32x16_bf16 v[66:81], v[10:13], v[236:239], v[66:81]
	v_max3_f32 v173, v173, v125, v126
	s_waitcnt lgkmcnt(0)
	v_mfma_f32_32x32x16_bf16 v[66:81], v[14:17], v[198:201], v[66:81]
	v_max3_f32 v249, v249, v111, v112
	v_mfma_f32_4x4x4_16b_bf16 v[240:243], v[2:3], v[132:133], v[240:243]
	v_max3_f32 v173, v173, v127, v128
	v_mfma_f32_4x4x4_16b_bf16 v[244:247], v[4:5], v[132:133], v[244:247]
	v_mfma_f32_4x4x4_16b_bf16 v[240:243], v[6:7], v[132:133], v[240:243]
	v_max_f32 v249, v249, v113
	v_mfma_f32_4x4x4_16b_bf16 v[244:247], v[8:9], v[132:133], v[244:247]
	v_mfma_f32_4x4x4_16b_bf16 v[240:243], v[10:11], v[132:133], v[240:243]
	v_max_f32 v173, v173, v129
	v_mfma_f32_4x4x4_16b_bf16 v[244:247], v[12:13], v[132:133], v[244:247]
	v_mfma_f32_4x4x4_16b_bf16 v[240:243], v[14:15], v[132:133], v[240:243]
	v_max_f32 v173, v173, v249
	v_mfma_f32_4x4x4_16b_bf16 v[244:247], v[16:17], v[132:133], v[244:247]
	s_setprio 0
	s_barrier
	s_add_i32 s36, s36, 0x20000
	s_add_i32 s97, s97, 1
	s_cmpk_eq_i32 s97, 0x7e
	s_cbranch_scc1 .LBB0_290
	s_mov_b32 s14, s94
	s_mov_b32 s94, s18
	s_mov_b32 s18, s96
	s_mov_b32 s15, s95
	s_mov_b32 s95, s93
	s_mov_b32 s93, s37
	s_branch .LBB0_282

; #define ATT_SBAR() __builtin_amdgcn_sched_barrier(0)
; #define ATT_PK4(P, BASE, OUT) do { u32x4 w = {cvtpk(P[BASE + 0], P[BASE + 1]), cvtpk(P[BASE + 2], P[BASE + 3]), cvtpk(P[BASE + 4], P[BASE + 5]), cvtpk(P[BASE + 6], P[BASE + 7])}; \
;     OUT = *reinterpret_cast<bf16x8*>(&w); } while (0)
; #define ATT_LOAD_K(t) do { const unsigned so_ = (unsigned)(t) * (unsigned)(KVBLK * LDK * 2); sk0 = __builtin_bit_cast(bf16x8, __builtin_amdgcn_raw_buffer_load_b128(krs, koff, so_, 0)); \
;     if constexpr (DQK == 128) sk1 = __builtin_bit_cast(bf16x8, __builtin_amdgcn_raw_buffer_load_b128(krs, koff, so_ + (unsigned)(32 * LDK * 2), 0)); } while (0)
; #define ATT_LOAD_V(t) do { const unsigned so_ = (unsigned)(t) * (unsigned)(KVBLK * LDV * 2); sv0 = __builtin_bit_cast(bf16x8, __builtin_amdgcn_raw_buffer_load_b128(vrs, voff, so_, 0)); \
;     sv1 = __builtin_bit_cast(bf16x8, __builtin_amdgcn_raw_buffer_load_b128(vrs, voff, so_ + (unsigned)(32 * LDV * 2), 0)); } while (0)
; #define ATT_WRITE_K(so) do { *(bf16x8*)(K_lds + (so) + kswz<DQK>(kr, kc * 2)) = sk0; if constexpr (DQK == 128) *(bf16x8*)(K_lds + (so) + kswz<DQK>(32 + kr, kc * 2)) = sk1; } while (0)
; #define ATT_WRITE_V(so) do { *(bf16x8*)(V_lds + (so) + vst0) = sv0; *(bf16x8*)(V_lds + (so) + vst1) = sv1; } while (0)
; #define ATT_BAR() do { ATT_SBAR(); asm volatile("s_barrier" ::: "memory"); ATT_SBAR(); } while (0)
; #define ATT_VPAIR(buf, so, blk, ks) do { if constexpr (!(ABL & 8) && !(ABL & 32)) { buf[2 * (ks)] = vtr(vq0 + (so) + v_rd_off(blk, ks, 0)); buf[2 * (ks) + 1] = vtr(vq0 + (so) + v_rd_off(blk, ks, 1)); } } while (0)
; __device__ __forceinline__ void softmax_exp_pack(f32x16& p0, f32x16& p1, bf16x8& pa0, bf16x8& pa1, bf16x8& pa2, bf16x8& pa3) {
; #pragma unroll
;   for (int r = 0; r < 16; ++r) { p0[r] = __builtin_amdgcn_exp2f(p0[r]); p1[r] = __builtin_amdgcn_exp2f(p1[r]); }
;     ...
;   ATT_PK4(p0, 0, pa0); ATT_PK4(p0, 8, pa1); ATT_PK4(p1, 0, pa2); ATT_PK4(p1, 8, pa3);
;     ...
;     if constexpr (!(ABL & 4)) { ATT_WRITE_K(k2); ATT_WRITE_V(v1); }
;     ATT_SBAR();
; #pragma unroll
;     for (int ks = 0; ks < 4; ++ks) ATT_VPAIR(va, v0, 0, ks);
;     asm volatile("s_waitcnt lgkmcnt(8)" ::: "memory"); ATT_BAR();
;     ATT_XSECTION(true);
;     if constexpr (!(ABL & 4)) { const int tk = (t + 3 < NT) ? t + 3 : NT - 1, tv = (t + 2 < NT) ? t + 2 : NT - 1; ATT_LOAD_K(tk); ATT_LOAD_V(tv); }
.LBB0_298:
	v_add_u32_e32 v152, s49, v170
	v_add_u32_e32 v153, s50, v168
	v_add_u32_e32 v154, s50, v169
	s_waitcnt vmcnt(0)
	ds_write_b128 v152, v[224:227] offset:49152
	ds_write_b128 v153, v[228:231]
	ds_write_b128 v154, v[232:235]
	s_min_u32 s14, s90, 0x7c
	s_lshl_b32 s14, s14, 17
	s_add_i32 s19, s14, 0x60000
	s_add_i32 s92, s36, 0xffff0000
	s_mov_b32 s14, s10
	s_mov_b32 s15, s11
	buffer_load_dwordx4 v[224:227], v171, s[8:11], s19 offen
	buffer_load_dwordx4 v[228:231], v172, s[12:15], s92 offen
	buffer_load_dwordx4 v[232:235], v172, s[12:15], s36 offen
	v_exp_f32_e32 v98, v98
	v_exp_f32_e32 v114, v114
	v_exp_f32_e32 v99, v99
	v_exp_f32_e32 v115, v115
	v_exp_f32_e32 v100, v100
	v_exp_f32_e32 v101, v101
	v_exp_f32_e32 v102, v102
	v_exp_f32_e32 v103, v103
	v_exp_f32_e32 v106, v106
	v_exp_f32_e32 v107, v107
	v_exp_f32_e32 v116, v116
	v_exp_f32_e32 v117, v117
	v_exp_f32_e32 v118, v118
	v_exp_f32_e32 v119, v119
	v_exp_f32_e32 v104, v104
	v_exp_f32_e32 v120, v120
	v_exp_f32_e32 v105, v105
	v_exp_f32_e32 v121, v121
	v_exp_f32_e32 v122, v122
	v_exp_f32_e32 v123, v123
	v_exp_f32_e32 v108, v108
	v_exp_f32_e32 v124, v124
	v_exp_f32_e32 v109, v109
	v_exp_f32_e32 v125, v125
	v_exp_f32_e32 v110, v110
	v_exp_f32_e32 v126, v126
	v_exp_f32_e32 v111, v111
	v_exp_f32_e32 v127, v127
	v_exp_f32_e32 v112, v112
	v_exp_f32_e32 v128, v128
	v_exp_f32_e32 v113, v113
	v_exp_f32_e32 v129, v129
	v_cvt_pk_bf16_f32 v18, v98, v99
	v_cvt_pk_bf16_f32 v19, v100, v101
	v_cvt_pk_bf16_f32 v20, v102, v103
	v_cvt_pk_bf16_f32 v22, v106, v107
	v_cvt_pk_bf16_f32 v26, v114, v115
	v_cvt_pk_bf16_f32 v21, v104, v105
	v_cvt_pk_bf16_f32 v23, v108, v109
	v_cvt_pk_bf16_f32 v24, v110, v111
	v_cvt_pk_bf16_f32 v25, v112, v113
	v_cvt_pk_bf16_f32 v27, v116, v117
	v_cvt_pk_bf16_f32 v28, v118, v119
	v_cvt_pk_bf16_f32 v29, v120, v121
	v_cvt_pk_bf16_f32 v30, v122, v123
	v_cvt_pk_bf16_f32 v31, v124, v125
	v_cvt_pk_bf16_f32 v32, v126, v127
	v_cvt_pk_bf16_f32 v33, v128, v129
	v_add_u32_e32 v249, s18, v173
	ds_read_b128 v[152:155], v249 offset:49152
	ds_read_b128 v[156:159], v249 offset:53760
	ds_read_b128 v[160:163], v249 offset:49184
	ds_read_b128 v[176:179], v249 offset:53792
	s_waitcnt lgkmcnt(4)
	s_barrier
; #define ATT_SBAR() __builtin_amdgcn_sched_barrier(0)
; __device__ __forceinline__ float softmax_rowmax(const f32x16& p0, const f32x16& p1) {
;   const float m0 = p1[0] + 0.0f; float a, b;
;   asm("v_max3_f32 %0, %1, %2, %3\n\tv_max3_f32 %0, %0, %4, %5\n\tv_max3_f32 %0, %0, %6, %7\n\tv_max3_f32 %0, %0, %8, %9\n\t"
;       "v_max3_f32 %0, %0, %10, %11\n\tv_max3_f32 %0, %0, %12, %13\n\tv_max3_f32 %0, %0, %14, %15\n\tv_max3_f32 %0, %0, %16, %17"
;       : "=&v"(a) : "v"(m0), "v"(p0[0]), "v"(p0[1]), "v"(p0[2]), "v"(p0[3]), "v"(p0[4]), "v"(p0[5]), "v"(p0[6]), "v"(p0[7]), "v"(p0[8]), "v"(p0[9]), "v"(p0[10]), "v"(p0[11]), "v"(p0[12]), "v"(p0[13]), "v"(p0[14]), "v"(p0[15]));
;   asm("v_max3_f32 %0, %1, %2, %3\n\tv_max3_f32 %0, %0, %4, %5\n\tv_max3_f32 %0, %0, %6, %7\n\tv_max3_f32 %0, %0, %8, %9\n\t"
;       "v_max3_f32 %0, %0, %10, %11\n\tv_max3_f32 %0, %0, %12, %13\n\tv_max3_f32 %0, %0, %14, %15\n\tv_max_f32 %0, %0, %16"
;       : "=&v"(b) : "v"(a), "v"(p1[1]), "v"(p1[2]), "v"(p1[3]), "v"(p1[4]), "v"(p1[5]), "v"(p1[6]), "v"(p1[7]), "v"(p1[8]), "v"(p1[9]), "v"(p1[10]), "v"(p1[11]), "v"(p1[12]), "v"(p1[13]), "v"(p1[14]), "v"(p1[15]));
;   return b;
;     ...
;   for (int t = 0; t + 1 < NT; ++t) {
;     if constexpr (ABL & 1) { u32x4 w0 = {cvtpk(p0[0], p0[1]), cvtpk(p0[2], p0[3]), cvtpk(p0[4], p0[5]), cvtpk(p0[6], p0[7])}, w1 = {cvtpk(p0[8], p0[9]), cvtpk(p0[10], p0[11]), cvtpk(p0[12], p0[13]), cvtpk(p0[14], p0[15])};
;         u32x4 w2 = {cvtpk(p1[0], p1[1]), cvtpk(p1[2], p1[3]), cvtpk(p1[4], p1[5]), cvtpk(p1[6], p1[7])}, w3 = {cvtpk(p1[8], p1[9]), cvtpk(p1[10], p1[11]), cvtpk(p1[12], p1[13]), cvtpk(p1[14], p1[15])};
;         pa0 = *reinterpret_cast<bf16x8*>(&w0); pa1 = *reinterpret_cast<bf16x8*>(&w1); pa2 = *reinterpret_cast<bf16x8*>(&w2); pa3 = *reinterpret_cast<bf16x8*>(&w3); }
;     else { ATT_SOFTMAX(t == 0); }
;     if constexpr (!(ABL & 4)) { ATT_WRITE_K(k2); ATT_WRITE_V(v1); }
;     ATT_SBAR();
; #pragma unroll
;     for (int ks = 0; ks < 4; ++ks) ATT_VPAIR(va, v0, 0, ks);
;     asm volatile("s_waitcnt lgkmcnt(8)" ::: "memory"); ATT_BAR();
;     ATT_XSECTION(true);
;     if constexpr (!(ABL & 4)) { const int tk = (t + 3 < NT) ? t + 3 : NT - 1, tv = (t + 2 < NT) ? t + 2 : NT - 1; ATT_LOAD_K(tk); ATT_LOAD_V(tv); }
;     ATT_BAR();
;     { const int tk_ = k0; k0 = k1; k1 = k2; k2 = tk_; const int tv_ = v0; v0 = v1; v1 = v2; v2 = tv_; }
	s_setprio 2
	s_waitcnt lgkmcnt(3)
	v_mfma_f32_32x32x16_bf16 v[98:113], v[152:155], v[136:139], v[82:97]
	ds_read_b128 v[180:183], v249 offset:49216
	s_waitcnt lgkmcnt(3)
	v_mfma_f32_32x32x16_bf16 v[114:129], v[156:159], v[136:139], v[82:97]
	ds_read_b128 v[186:189], v249 offset:53824
	v_add_u32_e32 v248, s37, v131
	s_waitcnt lgkmcnt(3)
	v_mfma_f32_32x32x16_bf16 v[98:113], v[160:163], v[140:143], v[98:113]
	ds_read_b128 v[190:193], v249 offset:49248
	ds_read_b64_tr_b16 v[198:199], v248
	ds_read_b64_tr_b16 v[200:201], v248 offset:2048
	s_waitcnt lgkmcnt(5)
	v_mfma_f32_32x32x16_bf16 v[114:129], v[176:179], v[140:143], v[114:129]
	ds_read_b128 v[194:197], v249 offset:53856
	ds_read_b64_tr_b16 v[212:213], v248 offset:4096
	ds_read_b64_tr_b16 v[214:215], v248 offset:6144
	s_waitcnt lgkmcnt(7)
	v_mfma_f32_32x32x16_bf16 v[98:113], v[180:183], v[144:147], v[98:113]
	ds_read_b64_tr_b16 v[216:217], v248 offset:8192
	ds_read_b64_tr_b16 v[218:219], v248 offset:10240
	s_waitcnt lgkmcnt(8)
	v_mfma_f32_32x32x16_bf16 v[114:129], v[186:189], v[144:147], v[114:129]
	ds_read_b64_tr_b16 v[220:221], v248 offset:12288
	ds_read_b64_tr_b16 v[222:223], v248 offset:14336
	s_waitcnt lgkmcnt(9)
	v_mfma_f32_32x32x16_bf16 v[98:113], v[190:193], v[148:151], v[98:113]
	s_waitcnt lgkmcnt(6)
	v_mfma_f32_32x32x16_bf16 v[114:129], v[194:197], v[148:151], v[114:129]
	v_mfma_f32_32x32x16_bf16 v[66:81], v[18:21], v[198:201], v[66:81]
	ds_read_b64_tr_b16 v[236:237], v248 offset:512
	ds_read_b64_tr_b16 v[238:239], v248 offset:2560
	s_waitcnt lgkmcnt(6)
	v_mfma_f32_32x32x16_bf16 v[66:81], v[22:25], v[212:215], v[66:81]
	ds_read_b64_tr_b16 v[198:199], v248 offset:4608
	ds_read_b64_tr_b16 v[200:201], v248 offset:6656
	s_waitcnt lgkmcnt(6)
	v_mfma_f32_32x32x16_bf16 v[66:81], v[26:29], v[216:219], v[66:81]
	ds_read_b64_tr_b16 v[212:213], v248 offset:8704
	ds_read_b64_tr_b16 v[214:215], v248 offset:10752
	s_waitcnt lgkmcnt(6)
	v_mfma_f32_32x32x16_bf16 v[66:81], v[30:33], v[220:223], v[66:81]
	ds_read_b64_tr_b16 v[216:217], v248 offset:12800
	ds_read_b64_tr_b16 v[218:219], v248 offset:14848
	v_max3_f32 v249, v98, v99, v100
	s_waitcnt lgkmcnt(6)
	v_mfma_f32_32x32x16_bf16 v[50:65], v[18:21], v[236:239], v[50:65]
	ds_read_b64_tr_b16 v[220:221], v248 offset:1024
	ds_read_b64_tr_b16 v[222:223], v248 offset:3072
	v_max3_f32 v174, v114, v115, v116
	s_waitcnt lgkmcnt(6)
	v_mfma_f32_32x32x16_bf16 v[50:65], v[22:25], v[198:201], v[50:65]
	ds_read_b64_tr_b16 v[236:237], v248 offset:5120
	ds_read_b64_tr_b16 v[238:239], v248 offset:7168
	v_max3_f32 v249, v249, v101, v102
	s_waitcnt lgkmcnt(6)
	v_mfma_f32_32x32x16_bf16 v[50:65], v[26:29], v[212:215], v[50:65]
	ds_read_b64_tr_b16 v[198:199], v248 offset:9216
	ds_read_b64_tr_b16 v[200:201], v248 offset:11264
	v_max3_f32 v174, v174, v117, v118
	s_waitcnt lgkmcnt(6)
	v_mfma_f32_32x32x16_bf16 v[50:65], v[30:33], v[216:219], v[50:65]
	ds_read_b64_tr_b16 v[212:213], v248 offset:13312
	ds_read_b64_tr_b16 v[214:215], v248 offset:15360
	v_max3_f32 v249, v249, v103, v104
	s_waitcnt lgkmcnt(6)
	v_mfma_f32_32x32x16_bf16 v[34:49], v[18:21], v[220:223], v[34:49]
	ds_read_b64_tr_b16 v[216:217], v248 offset:1536
	ds_read_b64_tr_b16 v[218:219], v248 offset:3584
	v_max3_f32 v174, v174, v119, v120
	s_waitcnt lgkmcnt(6)
	v_mfma_f32_32x32x16_bf16 v[34:49], v[22:25], v[236:239], v[34:49]
	ds_read_b64_tr_b16 v[220:221], v248 offset:5632
	ds_read_b64_tr_b16 v[222:223], v248 offset:7680
	v_max3_f32 v249, v249, v105, v106
	s_waitcnt lgkmcnt(6)
	v_mfma_f32_32x32x16_bf16 v[34:49], v[26:29], v[198:201], v[34:49]
	ds_read_b64_tr_b16 v[236:237], v248 offset:9728
	ds_read_b64_tr_b16 v[238:239], v248 offset:11776
	v_max3_f32 v174, v174, v121, v122
	s_waitcnt lgkmcnt(6)
	v_mfma_f32_32x32x16_bf16 v[34:49], v[30:33], v[212:215], v[34:49]
	ds_read_b64_tr_b16 v[198:199], v248 offset:13824
	ds_read_b64_tr_b16 v[200:201], v248 offset:15872
	v_max3_f32 v249, v249, v107, v108
	s_waitcnt lgkmcnt(6)
	v_mfma_f32_32x32x16_bf16 v[2:17], v[18:21], v[216:219], v[2:17]
	v_max3_f32 v174, v174, v123, v124
	s_waitcnt lgkmcnt(4)
	v_mfma_f32_32x32x16_bf16 v[2:17], v[22:25], v[220:223], v[2:17]
	v_max3_f32 v249, v249, v109, v110
	s_waitcnt lgkmcnt(2)
	v_mfma_f32_32x32x16_bf16 v[2:17], v[26:29], v[236:239], v[2:17]
	v_max3_f32 v174, v174, v125, v126
	s_waitcnt lgkmcnt(0)
	v_mfma_f32_32x32x16_bf16 v[2:17], v[30:33], v[198:201], v[2:17]
	v_max3_f32 v249, v249, v111, v112
	v_mfma_f32_4x4x4_16b_bf16 v[240:243], v[18:19], v[132:133], v[240:243]
	v_max3_f32 v174, v174, v127, v128
	v_mfma_f32_4x4x4_16b_bf16 v[244:247], v[20:21], v[132:133], v[244:247]
	v_mfma_f32_4x4x4_16b_bf16 v[240:243], v[22:23], v[132:133], v[240:243]
	v_max_f32 v249, v249, v113
	v_mfma_f32_4x4x4_16b_bf16 v[244:247], v[24:25], v[132:133], v[244:247]
	v_mfma_f32_4x4x4_16b_bf16 v[240:243], v[26:27], v[132:133], v[240:243]
	v_max_f32 v174, v174, v129
	v_mfma_f32_4x4x4_16b_bf16 v[244:247], v[28:29], v[132:133], v[244:247]
	v_mfma_f32_4x4x4_16b_bf16 v[240:243], v[30:31], v[132:133], v[240:243]
	v_max_f32 v174, v174, v249
	v_mfma_f32_4x4x4_16b_bf16 v[244:247], v[32:33], v[132:133], v[244:247]
	s_setprio 0
	s_barrier
	s_add_i32 s36, s36, 0x20000
	s_add_i32 s90, s90, 1
	s_cmpk_eq_i32 s90, 0x7e
	s_cbranch_scc1 .LBB0_305
	s_mov_b32 s14, s49
	s_mov_b32 s49, s51
	s_mov_b32 s51, s18
	s_mov_b32 s15, s50
	s_mov_b32 s50, s48
	s_mov_b32 s48, s37
	s_branch .LBB0_297
